# HOUT: the four gain vectors of a unit loaded together and waited with vmcnt(3); no wait sits behind the result store just issued
# speedup vs baseline: 1.0087x; 1.0006x over previous
.LBB0_312:
	s_or_b64 exec, exec, s[4:5]
	s_waitcnt lgkmcnt(0)
	s_barrier
	ds_read2st64_b32 v[204:205], v197 offset1:1
	v_mad_i64_i32 v[178:179], s[4:5], v0, s89, 0
	v_lshl_add_u64 v[208:209], s[12:13], 0, v[178:179]
	v_lshl_add_u64 v[178:179], v[174:175], 2, s[10:11]
	s_waitcnt lgkmcnt(0)
	v_add_f32_e32 v0, v204, v205
	global_load_dwordx4 v[204:207], v[178:179], off
	global_load_dwordx4 v[236:239], v[178:179], off offset:64
	global_load_dwordx4 v[240:243], v[178:179], off offset:128
	global_load_dwordx4 v[244:247], v[178:179], off offset:192
	s_waitcnt vmcnt(7)
	v_lshlrev_b32_e32 v210, 16, v188
	v_and_b32_e32 v211, 0xffff0000, v188
	v_mul_f32_e32 v188, 0xbfb8aa3b, v210
	v_exp_f32_e32 v188, v188
	v_fmamk_f32 v0, v0, 0x3c000000, v224
	v_cmp_gt_f32_e32 vcc, s53, v0
	v_mul_f32_e32 v203, 0x4b800000, v0
	v_add_f32_e32 v188, 1.0, v188
	v_cndmask_b32_e32 v0, v0, v203, vcc
	v_rcp_f32_e32 v212, v188
	v_mul_f32_e32 v188, 0xbfb8aa3b, v211
	v_rsq_f32_e32 v0, v0
	v_exp_f32_e32 v188, v188
	v_lshl_add_u64 v[174:175], v[174:175], 1, v[208:209]
	v_mul_f32_e32 v203, 0x45800000, v0
	v_add_f32_e32 v188, 1.0, v188
	v_cndmask_b32_e32 v0, v0, v203, vcc
	v_rcp_f32_e32 v213, v188
	v_pk_mul_f32 v[192:193], v[192:193], v[0:1] op_sel_hi:[1,0]
	v_pk_mul_f32 v[190:191], v[190:191], v[0:1] op_sel_hi:[1,0]
	v_pk_mul_f32 v[186:187], v[186:187], v[0:1] op_sel_hi:[1,0]
	v_pk_mul_f32 v[184:185], v[184:185], v[0:1] op_sel_hi:[1,0]
	v_pk_mul_f32 v[180:181], v[180:181], v[0:1] op_sel_hi:[1,0]
	v_pk_mul_f32 v[176:177], v[176:177], v[0:1] op_sel_hi:[1,0]
	v_pk_mul_f32 v[170:171], v[170:171], v[0:1] op_sel_hi:[1,0]
	v_pk_mul_f32 v[168:169], v[168:169], v[0:1] op_sel_hi:[1,0]
	s_waitcnt vmcnt(3)
	v_pk_mul_f32 v[192:193], v[204:205], v[192:193]
	s_nop 0
	v_pk_mul_f32 v[192:193], v[192:193], v[210:211]
	v_pk_mul_f32 v[190:191], v[206:207], v[190:191]
	v_pk_mul_f32 v[192:193], v[212:213], v[192:193]
	s_nop 0
	v_cvt_pk_bf16_f32 v188, v192, v193
	v_lshlrev_b32_e32 v192, 16, v189
	v_and_b32_e32 v193, 0xffff0000, v189
	v_mul_f32_e32 v189, 0xbfb8aa3b, v192
	v_exp_f32_e32 v189, v189
	v_pk_mul_f32 v[190:191], v[190:191], v[192:193]
	v_lshlrev_b32_e32 v192, 16, v182
	v_add_f32_e32 v189, 1.0, v189
	v_rcp_f32_e32 v204, v189
	v_mul_f32_e32 v189, 0xbfb8aa3b, v193
	v_exp_f32_e32 v189, v189
	v_and_b32_e32 v193, 0xffff0000, v182
	v_mul_f32_e32 v182, 0xbfb8aa3b, v192
	v_exp_f32_e32 v182, v182
	v_add_f32_e32 v189, 1.0, v189
	v_rcp_f32_e32 v205, v189
	v_add_f32_e32 v182, 1.0, v182
	v_pk_mul_f32 v[190:191], v[204:205], v[190:191]
	s_nop 0
	v_cvt_pk_bf16_f32 v189, v190, v191
	global_store_dwordx2 v[174:175], v[188:189], off
	v_rcp_f32_e32 v204, v182
	v_mul_f32_e32 v182, 0xbfb8aa3b, v193
	v_exp_f32_e32 v182, v182
	s_waitcnt vmcnt(3)
	v_pk_mul_f32 v[186:187], v[236:237], v[186:187]
	v_add_f32_e32 v182, 1.0, v182
	v_rcp_f32_e32 v205, v182
	v_pk_mul_f32 v[186:187], v[186:187], v[192:193]
	v_pk_mul_f32 v[184:185], v[238:239], v[184:185]
	v_pk_mul_f32 v[186:187], v[204:205], v[186:187]
	s_nop 0
	v_cvt_pk_bf16_f32 v182, v186, v187
	v_lshlrev_b32_e32 v186, 16, v183
	v_and_b32_e32 v187, 0xffff0000, v183
	v_mul_f32_e32 v183, 0xbfb8aa3b, v186
	v_exp_f32_e32 v183, v183
	v_pk_mul_f32 v[184:185], v[184:185], v[186:187]
	v_lshlrev_b32_e32 v186, 16, v172
	v_add_f32_e32 v183, 1.0, v183
	v_rcp_f32_e32 v188, v183
	v_mul_f32_e32 v183, 0xbfb8aa3b, v187
	v_exp_f32_e32 v183, v183
	v_and_b32_e32 v187, 0xffff0000, v172
	v_mul_f32_e32 v172, 0xbfb8aa3b, v186
	v_exp_f32_e32 v172, v172
	v_add_f32_e32 v183, 1.0, v183
	v_rcp_f32_e32 v189, v183
	v_add_f32_e32 v172, 1.0, v172
	v_pk_mul_f32 v[184:185], v[188:189], v[184:185]
	s_nop 0
	v_cvt_pk_bf16_f32 v183, v184, v185
	global_store_dwordx2 v[174:175], v[182:183], off offset:32
	v_rcp_f32_e32 v188, v172
	v_mul_f32_e32 v172, 0xbfb8aa3b, v187
	v_exp_f32_e32 v172, v172
	s_waitcnt vmcnt(3)
	v_pk_mul_f32 v[180:181], v[240:241], v[180:181]
	v_add_f32_e32 v172, 1.0, v172
	v_rcp_f32_e32 v189, v172
	v_pk_mul_f32 v[180:181], v[180:181], v[186:187]
	v_pk_mul_f32 v[176:177], v[242:243], v[176:177]
	v_pk_mul_f32 v[180:181], v[188:189], v[180:181]
	s_nop 0
	v_cvt_pk_bf16_f32 v172, v180, v181
	v_lshlrev_b32_e32 v180, 16, v173
	v_and_b32_e32 v181, 0xffff0000, v173
	v_mul_f32_e32 v173, 0xbfb8aa3b, v180
	v_exp_f32_e32 v173, v173
	v_pk_mul_f32 v[176:177], v[176:177], v[180:181]
	v_add_f32_e32 v173, 1.0, v173
	v_rcp_f32_e32 v182, v173
	v_mul_f32_e32 v173, 0xbfb8aa3b, v181
	v_exp_f32_e32 v173, v173
	s_nop 0
	v_add_f32_e32 v173, 1.0, v173
	v_rcp_f32_e32 v183, v173
	s_nop 0
	v_pk_mul_f32 v[176:177], v[182:183], v[176:177]
	s_nop 0
	v_cvt_pk_bf16_f32 v173, v176, v177
	global_store_dwordx2 v[174:175], v[172:173], off offset:64
	v_lshlrev_b32_e32 v172, 16, v166
	v_and_b32_e32 v173, 0xffff0000, v166
	v_mul_f32_e32 v166, 0xbfb8aa3b, v172
	v_exp_f32_e32 v166, v166
	s_waitcnt vmcnt(3)
	v_pk_mul_f32 v[170:171], v[244:245], v[170:171]
	v_add_f32_e32 v166, 1.0, v166
	v_rcp_f32_e32 v180, v166
	v_mul_f32_e32 v166, 0xbfb8aa3b, v173
	v_exp_f32_e32 v166, v166
	v_pk_mul_f32 v[170:171], v[170:171], v[172:173]
	v_pk_mul_f32 v[168:169], v[246:247], v[168:169]
	v_add_f32_e32 v166, 1.0, v166
	v_rcp_f32_e32 v181, v166
	s_nop 0
	v_pk_mul_f32 v[170:171], v[180:181], v[170:171]
	s_nop 0
	v_cvt_pk_bf16_f32 v166, v170, v171
	v_lshlrev_b32_e32 v170, 16, v167
	v_and_b32_e32 v171, 0xffff0000, v167
	v_mul_f32_e32 v167, 0xbfb8aa3b, v170
	v_mul_f32_e32 v0, 0xbfb8aa3b, v171
	v_exp_f32_e32 v167, v167
	v_exp_f32_e32 v0, v0
	v_pk_mul_f32 v[168:169], v[168:169], v[170:171]
	v_add_f32_e32 v167, 1.0, v167
	v_add_f32_e32 v0, 1.0, v0
	v_rcp_f32_e32 v172, v167
	v_rcp_f32_e32 v173, v0
	s_nop 0
	v_pk_mul_f32 v[168:169], v[172:173], v[168:169]
	s_nop 0
	v_cvt_pk_bf16_f32 v167, v168, v169
	global_store_dwordx2 v[174:175], v[166:167], off offset:96
	s_barrier

.LBB0_318:
	s_or_b64 exec, exec, s[4:5]
	s_waitcnt lgkmcnt(0)
	s_barrier
	ds_read2st64_b32 v[204:205], v197 offset1:1
	v_mad_i64_i32 v[176:177], s[4:5], v0, s89, 0
	v_lshl_add_u64 v[208:209], s[12:13], 0, v[176:177]
	v_lshl_add_u64 v[176:177], v[180:181], 2, s[10:11]
	s_waitcnt lgkmcnt(0)
	v_add_f32_e32 v0, v204, v205
	global_load_dwordx4 v[204:207], v[176:177], off
	global_load_dwordx4 v[236:239], v[176:177], off offset:64
	global_load_dwordx4 v[240:243], v[176:177], off offset:128
	global_load_dwordx4 v[244:247], v[176:177], off offset:192
	s_waitcnt vmcnt(7)
	v_lshlrev_b32_e32 v210, 16, v188
	v_and_b32_e32 v211, 0xffff0000, v188
	v_mul_f32_e32 v188, 0xbfb8aa3b, v210
	v_exp_f32_e32 v188, v188
	v_fmamk_f32 v0, v0, 0x3c000000, v224
	v_cmp_gt_f32_e32 vcc, s53, v0
	v_mul_f32_e32 v203, 0x4b800000, v0
	v_add_f32_e32 v188, 1.0, v188
	v_cndmask_b32_e32 v0, v0, v203, vcc
	v_rcp_f32_e32 v212, v188
	v_mul_f32_e32 v188, 0xbfb8aa3b, v211
	v_rsq_f32_e32 v0, v0
	v_exp_f32_e32 v188, v188
	v_lshl_add_u64 v[180:181], v[180:181], 1, v[208:209]
	v_mul_f32_e32 v203, 0x45800000, v0
	v_add_f32_e32 v188, 1.0, v188
	v_cndmask_b32_e32 v0, v0, v203, vcc
	v_rcp_f32_e32 v213, v188
	v_pk_mul_f32 v[192:193], v[192:193], v[0:1] op_sel_hi:[1,0]
	v_pk_mul_f32 v[190:191], v[190:191], v[0:1] op_sel_hi:[1,0]
	v_pk_mul_f32 v[186:187], v[186:187], v[0:1] op_sel_hi:[1,0]
	v_pk_mul_f32 v[184:185], v[184:185], v[0:1] op_sel_hi:[1,0]
	v_pk_mul_f32 v[178:179], v[178:179], v[0:1] op_sel_hi:[1,0]
	v_pk_mul_f32 v[174:175], v[174:175], v[0:1] op_sel_hi:[1,0]
	v_pk_mul_f32 v[170:171], v[170:171], v[0:1] op_sel_hi:[1,0]
	v_pk_mul_f32 v[168:169], v[168:169], v[0:1] op_sel_hi:[1,0]
	s_andn2_b64 vcc, exec, s[20:21]
	s_waitcnt vmcnt(3)
	v_pk_mul_f32 v[192:193], v[204:205], v[192:193]
	s_nop 0
	v_pk_mul_f32 v[192:193], v[192:193], v[210:211]
	v_pk_mul_f32 v[190:191], v[206:207], v[190:191]
	v_pk_mul_f32 v[192:193], v[212:213], v[192:193]
	s_nop 0
	v_cvt_pk_bf16_f32 v188, v192, v193
	v_lshlrev_b32_e32 v192, 16, v189
	v_and_b32_e32 v193, 0xffff0000, v189
	v_mul_f32_e32 v189, 0xbfb8aa3b, v192
	v_exp_f32_e32 v189, v189
	v_pk_mul_f32 v[190:191], v[190:191], v[192:193]
	v_lshlrev_b32_e32 v192, 16, v182
	v_add_f32_e32 v189, 1.0, v189
	v_rcp_f32_e32 v204, v189
	v_mul_f32_e32 v189, 0xbfb8aa3b, v193
	v_exp_f32_e32 v189, v189
	v_and_b32_e32 v193, 0xffff0000, v182
	v_mul_f32_e32 v182, 0xbfb8aa3b, v192
	v_exp_f32_e32 v182, v182
	v_add_f32_e32 v189, 1.0, v189
	v_rcp_f32_e32 v205, v189
	v_add_f32_e32 v182, 1.0, v182
	v_pk_mul_f32 v[190:191], v[204:205], v[190:191]
	s_nop 0
	v_cvt_pk_bf16_f32 v189, v190, v191
	global_store_dwordx2 v[180:181], v[188:189], off
	v_rcp_f32_e32 v204, v182
	v_mul_f32_e32 v182, 0xbfb8aa3b, v193
	v_exp_f32_e32 v182, v182
	s_waitcnt vmcnt(3)
	v_pk_mul_f32 v[186:187], v[236:237], v[186:187]
	v_add_f32_e32 v182, 1.0, v182
	v_rcp_f32_e32 v205, v182
	v_pk_mul_f32 v[186:187], v[186:187], v[192:193]
	v_pk_mul_f32 v[184:185], v[238:239], v[184:185]
	v_pk_mul_f32 v[186:187], v[204:205], v[186:187]
	s_nop 0
	v_cvt_pk_bf16_f32 v182, v186, v187
	v_lshlrev_b32_e32 v186, 16, v183
	v_and_b32_e32 v187, 0xffff0000, v183
	v_mul_f32_e32 v183, 0xbfb8aa3b, v186
	v_exp_f32_e32 v183, v183
	v_pk_mul_f32 v[184:185], v[184:185], v[186:187]
	v_lshlrev_b32_e32 v186, 16, v172
	v_add_f32_e32 v183, 1.0, v183
	v_rcp_f32_e32 v188, v183
	v_mul_f32_e32 v183, 0xbfb8aa3b, v187
	v_exp_f32_e32 v183, v183
	v_and_b32_e32 v187, 0xffff0000, v172
	v_mul_f32_e32 v172, 0xbfb8aa3b, v186
	v_exp_f32_e32 v172, v172
	v_add_f32_e32 v183, 1.0, v183
	v_rcp_f32_e32 v189, v183
	v_add_f32_e32 v172, 1.0, v172
	v_pk_mul_f32 v[184:185], v[188:189], v[184:185]
	s_nop 0
	v_cvt_pk_bf16_f32 v183, v184, v185
	global_store_dwordx2 v[180:181], v[182:183], off offset:32
	v_rcp_f32_e32 v188, v172
	v_mul_f32_e32 v172, 0xbfb8aa3b, v187
	v_exp_f32_e32 v172, v172
	s_waitcnt vmcnt(3)
	v_pk_mul_f32 v[178:179], v[240:241], v[178:179]
	v_add_f32_e32 v172, 1.0, v172
	v_rcp_f32_e32 v189, v172
	v_pk_mul_f32 v[178:179], v[178:179], v[186:187]
	v_pk_mul_f32 v[174:175], v[242:243], v[174:175]
	v_pk_mul_f32 v[178:179], v[188:189], v[178:179]
	s_nop 0
	v_cvt_pk_bf16_f32 v172, v178, v179
	v_lshlrev_b32_e32 v178, 16, v173
	v_and_b32_e32 v179, 0xffff0000, v173
	v_mul_f32_e32 v173, 0xbfb8aa3b, v178
	v_exp_f32_e32 v173, v173
	v_pk_mul_f32 v[174:175], v[174:175], v[178:179]
	v_add_f32_e32 v173, 1.0, v173
	v_rcp_f32_e32 v182, v173
	v_mul_f32_e32 v173, 0xbfb8aa3b, v179
	v_exp_f32_e32 v173, v173
	s_nop 0
	v_add_f32_e32 v173, 1.0, v173
	v_rcp_f32_e32 v183, v173
	s_nop 0
	v_pk_mul_f32 v[174:175], v[182:183], v[174:175]
	s_nop 0
	v_cvt_pk_bf16_f32 v173, v174, v175
	global_store_dwordx2 v[180:181], v[172:173], off offset:64
	v_lshlrev_b32_e32 v176, 16, v166
	v_and_b32_e32 v177, 0xffff0000, v166
	v_mul_f32_e32 v166, 0xbfb8aa3b, v176
	v_exp_f32_e32 v166, v166
	s_waitcnt vmcnt(3)
	v_pk_mul_f32 v[170:171], v[244:245], v[170:171]
	v_add_f32_e32 v166, 1.0, v166
	v_rcp_f32_e32 v178, v166
	v_mul_f32_e32 v166, 0xbfb8aa3b, v177
	v_exp_f32_e32 v166, v166
	v_pk_mul_f32 v[170:171], v[170:171], v[176:177]
	v_pk_mul_f32 v[168:169], v[246:247], v[168:169]
	v_add_f32_e32 v166, 1.0, v166
	v_rcp_f32_e32 v179, v166
	s_nop 0
	v_pk_mul_f32 v[170:171], v[178:179], v[170:171]
	s_nop 0
	v_cvt_pk_bf16_f32 v166, v170, v171
	v_lshlrev_b32_e32 v170, 16, v167
	v_and_b32_e32 v171, 0xffff0000, v167
	v_mul_f32_e32 v167, 0xbfb8aa3b, v170
	v_mul_f32_e32 v0, 0xbfb8aa3b, v171
	v_exp_f32_e32 v167, v167
	v_exp_f32_e32 v0, v0
	v_pk_mul_f32 v[168:169], v[168:169], v[170:171]
	v_add_f32_e32 v167, 1.0, v167
	v_add_f32_e32 v0, 1.0, v0
	v_rcp_f32_e32 v172, v167
	v_rcp_f32_e32 v173, v0
	s_nop 0
	v_pk_mul_f32 v[168:169], v[172:173], v[168:169]
	s_nop 0
	v_cvt_pk_bf16_f32 v167, v168, v169
	global_store_dwordx2 v[180:181], v[166:167], off offset:96
	s_barrier
	s_cbranch_vccnz .LBB0_313
	v_readlane_b32 s4, v254, 53
	s_add_i32 s4, s4, s22
	s_cmpk_gt_i32 s4, 0x5ff
	s_cbranch_scc1 .LBB0_321
	s_mul_hi_i32 s5, s4, 0x2aaaaaab
	s_lshr_b32 s19, s5, 31
	s_lshr_b32 s5, s5, 6
	s_add_i32 s19, s5, s19
	s_ashr_i32 s5, s4, 31
	s_lshr_b32 s20, s5, 26
	s_add_i32 s20, s4, s20
	s_ashr_i32 s21, s20, 6
	s_and_b32 s20, s20, 0x3ffffc0
	s_mul_hi_i32 s22, s21, 0x2aaaaaab
	s_sub_i32 s20, s4, s20
	s_lshr_b32 s23, s22, 31
	s_lshl_b32 s19, s19, 12
	s_lshl_b32 s20, s20, 6
	s_lshl_b64 s[4:5], s[4:5], 15
	s_add_i32 s22, s22, s23
	s_add_i32 s19, s19, s20
	v_lshl_add_u64 v[90:91], v[164:165], 0, s[4:5]
	s_mul_i32 s22, s22, 6
	v_or_b32_e32 v0, s19, v202
	v_mov_b64_e32 v[2:3], s[16:17]
	v_add_co_u32_e32 v42, vcc, s59, v90
	s_sub_i32 s22, s21, s22
	v_mad_i64_i32 v[2:3], s[20:21], v0, s89, v[2:3]
	v_addc_co_u32_e32 v43, vcc, 0, v91, vcc
	s_lshl_b32 s20, s22, 7
	v_add_co_u32_e32 v66, vcc, 0x2000, v90
	s_ashr_i32 s21, s20, 31
	s_nop 0
	v_addc_co_u32_e32 v67, vcc, 0, v91, vcc
	v_lshl_add_u64 v[2:3], s[20:21], 1, v[2:3]
	v_lshlrev_b32_e32 v0, 1, v162
	v_add_co_u32_e32 v110, vcc, 0x3000, v90
	v_lshl_add_u64 v[14:15], v[2:3], 0, v[0:1]
	s_nop 0
	v_addc_co_u32_e32 v111, vcc, 0, v91, vcc
	global_load_dwordx4 v[2:5], v[14:15], off
	global_load_dwordx4 v[6:9], v[14:15], off offset:64
	global_load_dwordx4 v[10:13], v[14:15], off offset:128
	s_nop 0
	global_load_dwordx4 v[14:17], v[14:15], off offset:192
	s_nop 0
	global_load_dwordx4 v[18:21], v[90:91], off
	global_load_dwordx4 v[22:25], v[90:91], off offset:64
	global_load_dwordx4 v[26:29], v[90:91], off offset:128
	global_load_dwordx4 v[30:33], v[90:91], off offset:192
	global_load_dwordx4 v[54:57], v[42:43], off
	global_load_dwordx4 v[34:37], v[42:43], off offset:64
	global_load_dwordx4 v[38:41], v[42:43], off offset:128
	s_nop 0
	global_load_dwordx4 v[42:45], v[42:43], off offset:192
	s_nop 0
	global_load_dwordx4 v[46:49], v[66:67], off
	global_load_dwordx4 v[50:53], v[66:67], off offset:64
	global_load_dwordx4 v[58:61], v[66:67], off offset:128
	s_nop 0
	global_load_dwordx4 v[66:69], v[66:67], off offset:192
	s_nop 0
	global_load_dwordx4 v[90:93], v[110:111], off
	global_load_dwordx4 v[98:101], v[110:111], off offset:64
	global_load_dwordx4 v[106:109], v[110:111], off offset:128
	s_nop 0
	global_load_dwordx4 v[110:113], v[110:111], off offset:192
